# speedup vs baseline: 1.0167x; 1.0051x over previous
.Lmk_p72:
	v_mov_b64_e32 v[130:131], 0
	v_mov_b64_e32 v[132:133], 0
	v_mov_b64_e32 v[134:135], 0
	v_mov_b64_e32 v[136:137], 0
	v_mov_b64_e32 v[138:139], 0
	v_mov_b64_e32 v[140:141], 0
	v_mov_b64_e32 v[142:143], 0
	v_mov_b64_e32 v[144:145], 0
	v_and_b32_e32 v200, 1, v114
	v_cmp_eq_u32_e32 vcc, 1, v200
	s_nop 1
	v_cndmask_b32_e32 v124, v124, v174, vcc
	s_cmp_lt_u32 s38, 4
	s_cbranch_scc0 .Lmk_prio_done
	s_setprio 1

.LBB2_110:
.Lmk_gather:
	s_mov_b32 s30, s83
	v_lshl_or_b32 v10, v224, 7, v176
	v_lshl_or_b32 v14, v225, 7, v176
	s_cmp_lt_i32 s83, 17
	global_load_dwordx4 v[10:13], v10, s[28:29]
	global_load_dwordx4 v[14:17], v14, s[28:29]
	s_cbranch_scc1 .LBB2_68
	v_lshl_or_b32 v30, v226, 7, v176
	v_lshl_or_b32 v26, v227, 7, v176
	s_cmp_lt_i32 s83, 33
	global_load_dwordx4 v[30:33], v30, s[28:29]
	global_load_dwordx4 v[26:29], v26, s[28:29]
	s_cbranch_scc1 .LBB2_68
	v_lshl_or_b32 v2, v232, 7, v176
	v_lshl_or_b32 v6, v233, 7, v176
	v_lshl_or_b32 v18, v234, 7, v176
	v_lshl_or_b32 v22, v235, 7, v176
	global_load_dwordx4 v[2:5], v2, s[28:29]
	global_load_dwordx4 v[6:9], v6, s[28:29]
	global_load_dwordx4 v[18:21], v18, s[28:29]
	global_load_dwordx4 v[22:25], v22, s[28:29]

.LBB2_72:
.LBB2_74:
	s_add_i32 s34, s45, -1
	s_cmp_lg_u32 s49, s34
	s_cbranch_scc1 .Lmk_tail
	s_and_b64 vcc, exec, s[54:55]
	s_cbranch_vccz .Lmk_ma_ready
	s_waitcnt vmcnt(2)

.Lmk_half_iter:
	s_cmp_lt_i32 s66, 17
	s_cbranch_scc1 .Lmk_quarter_iter
	ds_read_b128 v[208:211], v122
	ds_read_b128 v[212:215], v117
	ds_read_b128 v[216:219], v122 offset:2048
	ds_read_b128 v[220:223], v117 offset:2048
	ds_read_b64_tr_b16 v[130:131], v186 offset:0
	ds_read_b64_tr_b16 v[132:133], v186 offset:2048
	ds_read_b64_tr_b16 v[134:135], v188 offset:0
	ds_read_b64_tr_b16 v[136:137], v188 offset:2048
	ds_read_b64_tr_b16 v[138:139], v189 offset:0
	ds_read_b64_tr_b16 v[140:141], v189 offset:2048
	ds_read_b64_tr_b16 v[142:143], v190 offset:0
	ds_read_b64_tr_b16 v[144:145], v190 offset:2048
	s_waitcnt lgkmcnt(8)
	v_mfma_f32_16x16x32_f16 v[200:203], v[240:243], v[208:211], 0
	v_mfma_f32_16x16x32_f16 v[160:163], v[240:243], v[216:219], 0
	v_mfma_f32_16x16x32_f16 v[200:203], v[244:247], v[212:215], v[200:203]
	v_mfma_f32_16x16x32_f16 v[160:163], v[244:247], v[220:223], v[160:163]
	s_nop 6
	s_branch .Lmk_half_join
.Lmk_quarter_iter:
	ds_read_b128 v[208:211], v122
	ds_read_b128 v[212:215], v117
	ds_read_b64_tr_b16 v[130:131], v186 offset:0
	ds_read_b64_tr_b16 v[134:135], v188 offset:0
	ds_read_b64_tr_b16 v[138:139], v189 offset:0
	ds_read_b64_tr_b16 v[142:143], v190 offset:0
	s_waitcnt lgkmcnt(4)
	v_mfma_f32_16x16x32_f16 v[200:203], v[240:243], v[208:211], 0
	v_mfma_f32_16x16x32_f16 v[200:203], v[244:247], v[212:215], v[200:203]
	s_nop 6
	s_branch .Lmk_half_join
